# fused W_out epilogue pass 1: both column halves of a row group loaded together (ring regs), plus DPP butterflies in norm/epilogue phases
# baseline (speedup 1.0000x reference)
; #define LAS __attribute__((address_space(3)))
; __device__ __forceinline__ float bflo(unsigned u) { return __uint_as_float(u << 16); }
; __device__ __forceinline__ float bfhi(unsigned u) { return __uint_as_float(u & 0xffff0000u); }
;     __device__ __forceinline__ void fused(AccT& acc, const GUnit& u, int wr, int wc, int fr, int fq, LAS unsigned char* lds, int wid, int lane) const {
;         const int b = u.pm >> 3, tid = wid * 64 + lane;
;         const int col0 = u.pn * 256 + wc * 32 + 8 * fq;
;         LAS float* P = (LAS float*)lds;
;         LAS float* S = (LAS float*)(lds + 4096);
;         LAS float* LP = (LAS float*)(lds + 8192);
;         f32x4 G[2][2];
; #pragma unroll
;         for (int bj = 0; bj < 2; ++bj)
; #pragma unroll
;             for (int n = 0; n < 2; ++n) { const int c = col0 + bj * 128 + n * 4; G[bj][n] = *(const f32x4*)(g2 + c) * (*(const f32x4*)(shf + (size_t)b * 12288 + 2048 + c) + 1.f); }
;         bf16x8 wf[2];
; #pragma unroll
;         for (int bj = 0; bj < 2; ++bj) wf[bj] = *(const bf16x8*)(WRT + (size_t)fr * 2048 + col0 + bj * 128);
;         {
;             f32x4 g[2][2];
; #pragma unroll
;             for (int bj = 0; bj < 2; ++bj)
; #pragma unroll
;                 for (int n = 0; n < 2; ++n) g[bj][n] = *(const f32x4*)(gate + (size_t)b * 12288 + col0 + bj * 128 + n * 4);
; #pragma unroll
;             for (int ai = 0; ai < 2; ++ai)
; #pragma unroll
;                 for (int m = 0; m < 4; ++m) {
;                     const size_t ro = (size_t)(u.pm * 256 + ai * 128 + wr * 64 + m * 16 + fr) * DM + col0;
; #pragma unroll
;                     for (int bj = 0; bj < 2; ++bj) {
;                         f32x4 x0, x1;
;                         if (base32) { x0 = *(const f32x4*)(base32 + ro + bj * 128); x1 = *(const f32x4*)(base32 + ro + bj * 128 + 4); }
;                         else { const u32x4 w = *(const u32x4*)(base16 + ro + bj * 128); x0 = (f32x4){bflo(w.x), bfhi(w.x), bflo(w.y), bfhi(w.y)}; x1 = (f32x4){bflo(w.z), bfhi(w.z), bflo(w.w), bfhi(w.w)}; }
.LBB0_1189:
	v_readlane_b32 s28, v250, 59
	v_readlane_b32 s29, v250, 60
	v_readlane_b32 s68, v249, 29
	s_lshl_b32 s33, s59, 5
	s_lshl_b64 s[48:49], s[28:29], 13
	v_readlane_b32 s80, v249, 41
	v_readlane_b32 s81, v249, 42
	s_add_u32 s12, s80, s48
	s_addc_u32 s13, s81, s49
	s_lshl_b64 s[28:29], s[28:29], 16
	v_readlane_b32 s34, v249, 55
	v_readlane_b32 s35, v249, 56
	s_add_u32 s28, s34, s28
	s_addc_u32 s29, s35, s29
	v_readlane_b32 s34, v255, 18
	s_mov_b32 s0, s34
	s_ashr_i32 s44, s34, 3
	v_readlane_b32 s34, v255, 17
	s_lshl_b32 s34, s34, 8
	v_bfe_u32 v208, v207, 4, 2
	s_or_b32 s33, s34, s33
	s_mul_i32 s45, s44, 0xc000
	v_lshl_or_b32 v196, v208, 3, s33
	s_mul_hi_i32 s33, s44, 0xc000
	s_add_u32 s11, s11, s45
	s_addc_u32 s22, s22, s33
	s_add_u32 s50, s11, 0x6000
	s_addc_u32 s51, s22, 0
	v_readlane_b32 s35, v255, 19
	s_add_u32 s34, s11, 0x8000
	v_ashrrev_i32_e32 v197, 31, v196
	s_addc_u32 s35, s22, 0
	v_lshlrev_b64 v[78:79], 2, v[196:197]
	v_lshl_add_u64 v[2:3], s[12:13], 0, v[78:79]
	v_lshl_add_u64 v[4:5], s[34:35], 0, v[78:79]
	s_waitcnt vmcnt(0)
	s_barrier
	global_load_dwordx4 v[94:97], v[2:3], off offset:16
	global_load_dwordx4 v[114:117], v[2:3], off
	global_load_dwordx4 v[106:109], v[4:5], off offset:16
	global_load_dwordx4 v[118:121], v[4:5], off
	v_or_b32_e32 v4, 0x80, v196
	v_ashrrev_i32_e32 v5, 31, v4
	global_load_dwordx4 v[82:85], v[2:3], off offset:528
	global_load_dwordx4 v[102:105], v[2:3], off offset:512
	v_lshl_add_u64 v[2:3], v[4:5], 2, s[34:35]
	v_lshlrev_b32_e32 v194, 12, v206
	s_add_u32 s12, s9, s45
	global_load_dwordx4 v[90:93], v[2:3], off offset:16
	global_load_dwordx4 v[110:113], v[2:3], off
	v_lshl_add_u64 v[2:3], s[28:29], 0, v[194:195]
	s_addc_u32 s13, s10, s33
	v_lshl_add_u64 v[2:3], v[196:197], 1, v[2:3]
	v_lshl_add_u64 v[98:99], s[12:13], 0, v[78:79]
	global_load_dwordx4 v[6:9], v[2:3], off
	s_nop 0
	global_load_dwordx4 v[2:5], v[2:3], off offset:256
	s_nop 0
	global_load_dwordx4 v[130:133], v[98:99], off offset:16
	global_load_dwordx4 v[134:137], v[98:99], off
	global_load_dwordx4 v[78:81], v[98:99], off offset:528
	s_nop 0
	global_load_dwordx4 v[98:101], v[98:99], off offset:512
	s_lshl_b32 s9, s0, 8
	s_add_i32 s10, s9, s23
	v_or_b32_e32 v198, s10, v206
	v_ashrrev_i32_e32 v199, 31, v198
	v_lshlrev_b64 v[186:187], 11, v[198:199]
	v_lshl_add_u64 v[204:205], v[186:187], 0, v[196:197]
	v_cndmask_b32_e64 v186, 0, 1, s[42:43]
	v_cmp_ne_u32_e64 s[34:35], 1, v186
	s_andn2_b64 vcc, exec, s[42:43]
	v_lshl_add_u64 v[200:201], v[204:205], 2, s[40:41]
	v_readlane_b32 s69, v249, 30
	v_readlane_b32 s70, v249, 31
	v_readlane_b32 s71, v249, 32
	v_readlane_b32 s72, v249, 33
	v_readlane_b32 s73, v249, 34
	v_readlane_b32 s74, v249, 35
	v_readlane_b32 s75, v249, 36
	v_readlane_b32 s76, v249, 37
	v_readlane_b32 s77, v249, 38
	v_readlane_b32 s78, v249, 39
	v_readlane_b32 s79, v249, 40
	v_readlane_b32 s82, v249, 43
	v_readlane_b32 s83, v249, 44
	s_cbranch_vccnz .LBB0_1191
	global_load_dwordx4 v[186:189], v[200:201], off offset:16
	global_load_dwordx4 v[190:193], v[200:201], off
	global_load_dwordx4 v[230:233], v[200:201], off offset:528
	global_load_dwordx4 v[234:237], v[200:201], off offset:512
	s_mov_b64 s[12:13], 0
	s_branch .LBB0_1192

; __device__ __forceinline__ unsigned pk2(float lo, float hi) { unsigned r; asm("v_cvt_pk_bf16_f32 %0, %1, %2" : "=v"(r) : "v"(lo), "v"(hi)); return r; }
; __device__ __forceinline__ float bflo(unsigned u) { return __uint_as_float(u << 16); }
; __device__ __forceinline__ float bfhi(unsigned u) { return __uint_as_float(u & 0xffff0000u); }
;     __device__ __forceinline__ void fused(AccT& acc, const GUnit& u, int wr, int wc, int fr, int fq, LAS unsigned char* lds, int wid, int lane) const {
;     ...
; #pragma unroll
;             for (int ai = 0; ai < 2; ++ai)
; #pragma unroll
;                 for (int m = 0; m < 4; ++m) {
;                     const size_t ro = (size_t)(u.pm * 256 + ai * 128 + wr * 64 + m * 16 + fr) * DM + col0;
; #pragma unroll
;                     for (int bj = 0; bj < 2; ++bj) {
;                         f32x4 x0, x1;
;                         if (base32) { x0 = *(const f32x4*)(base32 + ro + bj * 128); x1 = *(const f32x4*)(base32 + ro + bj * 128 + 4); }
;                         else { const u32x4 w = *(const u32x4*)(base16 + ro + bj * 128); x0 = (f32x4){bflo(w.x), bfhi(w.x), bflo(w.y), bfhi(w.y)}; x1 = (f32x4){bflo(w.z), bfhi(w.z), bflo(w.w), bfhi(w.w)}; }
;                         const f32x4 v0 = x0 + g[bj][0] * acc[ai][bj][m][0], v1 = x1 + g[bj][1] * acc[ai][bj][m][1];
;                         acc[ai][bj][m][0] = v0; acc[ai][bj][m][1] = v1;
;                         u32x4 o; o.x = pk2(v0[0], v0[1]); o.y = pk2(v0[2], v0[3]); o.z = pk2(v1[0], v1[1]); o.w = pk2(v1[2], v1[3]);
;                         *(u32x4*)(X2 + ro + bj * 128) = o;
;                     }
.LBB0_1192:
	v_readlane_b32 s10, v250, 0
	v_readlane_b32 s11, v250, 1
	s_andn2_b64 vcc, exec, s[12:13]
	s_nop 0
	v_lshl_add_u64 v[202:203], v[204:205], 1, s[10:11]
	s_cbranch_vccnz .LBB0_1194
	global_load_dwordx4 v[186:189], v[202:203], off
	global_load_dwordx4 v[230:233], v[202:203], off offset:256
	s_waitcnt vmcnt(1)
	v_lshlrev_b32_e32 v190, 16, v186
	v_and_b32_e32 v191, 0xffff0000, v186
	v_lshlrev_b32_e32 v192, 16, v187
	v_and_b32_e32 v193, 0xffff0000, v187
	v_lshlrev_b32_e32 v186, 16, v188
	v_and_b32_e32 v187, 0xffff0000, v188
	v_lshlrev_b32_e32 v188, 16, v189
	v_and_b32_e32 v189, 0xffff0000, v189
.LBB0_1194:
	v_readlane_b32 s10, v249, 62
	v_readlane_b32 s11, v249, 63
	s_waitcnt vmcnt(2)
	v_pk_fma_f32 v[192:193], v[184:185], v[136:137], v[192:193]
	v_pk_fma_f32 v[190:191], v[182:183], v[134:135], v[190:191]
	v_pk_fma_f32 v[188:189], v[180:181], v[132:133], v[188:189]
	v_pk_fma_f32 v[186:187], v[178:179], v[130:131], v[186:187]
	v_lshl_add_u64 v[204:205], v[204:205], 1, s[10:11]
	s_and_b64 vcc, exec, s[34:35]
	v_cvt_pk_bf16_f32 v178, v190, v191
	v_cvt_pk_bf16_f32 v179, v192, v193
	v_cvt_pk_bf16_f32 v180, v186, v187
	v_cvt_pk_bf16_f32 v181, v188, v189
	global_store_dwordx4 v[204:205], v[178:181], off
	s_cbranch_vccnz .LBB0_1199
	s_nop 1
	s_waitcnt vmcnt(1)
	v_mov_b32_e32 v178, v230
	v_mov_b32_e32 v179, v231
	v_mov_b32_e32 v180, v232
	v_mov_b32_e32 v181, v233
	v_mov_b32_e32 v182, v234
	v_mov_b32_e32 v183, v235
	v_mov_b32_e32 v184, v236
	v_mov_b32_e32 v185, v237
	s_cbranch_execnz .LBB0_1197
.LBB0_1196:
	s_waitcnt vmcnt(1)
	v_lshlrev_b32_e32 v182, 16, v230
	v_and_b32_e32 v183, 0xffff0000, v230
	v_lshlrev_b32_e32 v184, 16, v231
	v_and_b32_e32 v185, 0xffff0000, v231
	v_lshlrev_b32_e32 v178, 16, v232
	v_and_b32_e32 v179, 0xffff0000, v232
	v_lshlrev_b32_e32 v180, 16, v233
	v_and_b32_e32 v181, 0xffff0000, v233
.LBB0_1197:
	s_waitcnt vmcnt(1)
	v_pk_fma_f32 v[182:183], v[174:175], v[98:99], v[182:183]
	v_pk_fma_f32 v[178:179], v[170:171], v[78:79], v[178:179]
	v_cvt_pk_bf16_f32 v170, v182, v183
	v_pk_fma_f32 v[184:185], v[176:177], v[100:101], v[184:185]
	v_pk_fma_f32 v[180:181], v[172:173], v[80:81], v[180:181]
	v_cvt_pk_bf16_f32 v171, v184, v185
	v_cvt_pk_bf16_f32 v172, v178, v179
	s_and_b64 vcc, exec, s[34:35]
	v_cvt_pk_bf16_f32 v173, v180, v181
	global_store_dwordx4 v[204:205], v[170:173], off offset:256
	s_nop 1
	v_or_b32_e32 v170, 16, v198
	v_ashrrev_i32_e32 v171, 31, v170
	v_lshlrev_b64 v[170:171], 11, v[170:171]
	v_lshl_add_u64 v[204:205], v[170:171], 0, v[196:197]
	v_lshl_add_u64 v[200:201], v[204:205], 2, s[40:41]
	s_cbranch_vccnz .LBB0_1200
	global_load_dwordx4 v[170:173], v[200:201], off offset:16
	global_load_dwordx4 v[174:177], v[200:201], off
	global_load_dwordx4 v[230:233], v[200:201], off offset:528
	global_load_dwordx4 v[234:237], v[200:201], off offset:512
	s_mov_b64 s[12:13], 0
	s_branch .LBB0_1201

; __device__ __forceinline__ unsigned pk2(float lo, float hi) { unsigned r; asm("v_cvt_pk_bf16_f32 %0, %1, %2" : "=v"(r) : "v"(lo), "v"(hi)); return r; }
; __device__ __forceinline__ float bflo(unsigned u) { return __uint_as_float(u << 16); }
; __device__ __forceinline__ float bfhi(unsigned u) { return __uint_as_float(u & 0xffff0000u); }
;     __device__ __forceinline__ void fused(AccT& acc, const GUnit& u, int wr, int wc, int fr, int fq, LAS unsigned char* lds, int wid, int lane) const {
;     ...
; #pragma unroll
;             for (int ai = 0; ai < 2; ++ai)
; #pragma unroll
;                 for (int m = 0; m < 4; ++m) {
;                     const size_t ro = (size_t)(u.pm * 256 + ai * 128 + wr * 64 + m * 16 + fr) * DM + col0;
; #pragma unroll
;                     for (int bj = 0; bj < 2; ++bj) {
;                         f32x4 x0, x1;
;                         if (base32) { x0 = *(const f32x4*)(base32 + ro + bj * 128); x1 = *(const f32x4*)(base32 + ro + bj * 128 + 4); }
;                         else { const u32x4 w = *(const u32x4*)(base16 + ro + bj * 128); x0 = (f32x4){bflo(w.x), bfhi(w.x), bflo(w.y), bfhi(w.y)}; x1 = (f32x4){bflo(w.z), bfhi(w.z), bflo(w.w), bfhi(w.w)}; }
;                         const f32x4 v0 = x0 + g[bj][0] * acc[ai][bj][m][0], v1 = x1 + g[bj][1] * acc[ai][bj][m][1];
;                         acc[ai][bj][m][0] = v0; acc[ai][bj][m][1] = v1;
;                         u32x4 o; o.x = pk2(v0[0], v0[1]); o.y = pk2(v0[2], v0[3]); o.z = pk2(v1[0], v1[1]); o.w = pk2(v1[2], v1[3]);
;                         *(u32x4*)(X2 + ro + bj * 128) = o;
;                     }
.LBB0_1201:
	v_readlane_b32 s10, v250, 0
	v_readlane_b32 s11, v250, 1
	s_andn2_b64 vcc, exec, s[12:13]
	s_nop 0
	v_lshl_add_u64 v[202:203], v[204:205], 1, s[10:11]
	s_cbranch_vccnz .LBB0_1203
	global_load_dwordx4 v[170:173], v[202:203], off
	global_load_dwordx4 v[230:233], v[202:203], off offset:256
	s_waitcnt vmcnt(1)
	v_lshlrev_b32_e32 v174, 16, v170
	v_and_b32_e32 v175, 0xffff0000, v170
	v_lshlrev_b32_e32 v176, 16, v171
	v_and_b32_e32 v177, 0xffff0000, v171
	v_lshlrev_b32_e32 v170, 16, v172
	v_and_b32_e32 v171, 0xffff0000, v172
	v_lshlrev_b32_e32 v172, 16, v173
	v_and_b32_e32 v173, 0xffff0000, v173
.LBB0_1203:
	v_readlane_b32 s10, v249, 62
	v_readlane_b32 s11, v249, 63
	s_waitcnt vmcnt(2)
	v_pk_fma_f32 v[176:177], v[168:169], v[136:137], v[176:177]
	v_pk_fma_f32 v[174:175], v[166:167], v[134:135], v[174:175]
	v_pk_fma_f32 v[172:173], v[164:165], v[132:133], v[172:173]
	v_pk_fma_f32 v[170:171], v[162:163], v[130:131], v[170:171]
	v_lshl_add_u64 v[204:205], v[204:205], 1, s[10:11]
	s_and_b64 vcc, exec, s[34:35]
	v_cvt_pk_bf16_f32 v162, v174, v175
	v_cvt_pk_bf16_f32 v163, v176, v177
	v_cvt_pk_bf16_f32 v164, v170, v171
	v_cvt_pk_bf16_f32 v165, v172, v173
	global_store_dwordx4 v[204:205], v[162:165], off
	s_cbranch_vccnz .LBB0_1208
	s_nop 1
	s_waitcnt vmcnt(1)
	v_mov_b32_e32 v162, v230
	v_mov_b32_e32 v163, v231
	v_mov_b32_e32 v164, v232
	v_mov_b32_e32 v165, v233
	v_mov_b32_e32 v166, v234
	v_mov_b32_e32 v167, v235
	v_mov_b32_e32 v168, v236
	v_mov_b32_e32 v169, v237
	s_cbranch_execnz .LBB0_1206
.LBB0_1205:
	s_waitcnt vmcnt(1)
	v_lshlrev_b32_e32 v166, 16, v230
	v_and_b32_e32 v167, 0xffff0000, v230
	v_lshlrev_b32_e32 v168, 16, v231
	v_and_b32_e32 v169, 0xffff0000, v231
	v_lshlrev_b32_e32 v162, 16, v232
	v_and_b32_e32 v163, 0xffff0000, v232
	v_lshlrev_b32_e32 v164, 16, v233
	v_and_b32_e32 v165, 0xffff0000, v233
.LBB0_1206:
	s_waitcnt vmcnt(1)
	v_pk_fma_f32 v[166:167], v[158:159], v[98:99], v[166:167]
	v_pk_fma_f32 v[162:163], v[154:155], v[78:79], v[162:163]
	v_cvt_pk_bf16_f32 v154, v166, v167
	v_pk_fma_f32 v[168:169], v[160:161], v[100:101], v[168:169]
	v_pk_fma_f32 v[164:165], v[156:157], v[80:81], v[164:165]
	v_cvt_pk_bf16_f32 v155, v168, v169
	v_cvt_pk_bf16_f32 v156, v162, v163
	s_and_b64 vcc, exec, s[34:35]
	v_cvt_pk_bf16_f32 v157, v164, v165
	global_store_dwordx4 v[204:205], v[154:157], off offset:256
	s_nop 1
	v_or_b32_e32 v154, 32, v198
	v_ashrrev_i32_e32 v155, 31, v154
	v_lshlrev_b64 v[154:155], 11, v[154:155]
	v_lshl_add_u64 v[204:205], v[154:155], 0, v[196:197]
	v_lshl_add_u64 v[200:201], v[204:205], 2, s[40:41]
	s_cbranch_vccnz .LBB0_1209
	global_load_dwordx4 v[154:157], v[200:201], off offset:16
	global_load_dwordx4 v[158:161], v[200:201], off
	global_load_dwordx4 v[230:233], v[200:201], off offset:528
	global_load_dwordx4 v[234:237], v[200:201], off offset:512
	s_mov_b64 s[12:13], 0
	s_branch .LBB0_1210

; __device__ __forceinline__ unsigned pk2(float lo, float hi) { unsigned r; asm("v_cvt_pk_bf16_f32 %0, %1, %2" : "=v"(r) : "v"(lo), "v"(hi)); return r; }
; __device__ __forceinline__ float bflo(unsigned u) { return __uint_as_float(u << 16); }
; __device__ __forceinline__ float bfhi(unsigned u) { return __uint_as_float(u & 0xffff0000u); }
;     __device__ __forceinline__ void fused(AccT& acc, const GUnit& u, int wr, int wc, int fr, int fq, LAS unsigned char* lds, int wid, int lane) const {
;     ...
; #pragma unroll
;             for (int ai = 0; ai < 2; ++ai)
; #pragma unroll
;                 for (int m = 0; m < 4; ++m) {
;                     const size_t ro = (size_t)(u.pm * 256 + ai * 128 + wr * 64 + m * 16 + fr) * DM + col0;
; #pragma unroll
;                     for (int bj = 0; bj < 2; ++bj) {
;                         f32x4 x0, x1;
;                         if (base32) { x0 = *(const f32x4*)(base32 + ro + bj * 128); x1 = *(const f32x4*)(base32 + ro + bj * 128 + 4); }
;                         else { const u32x4 w = *(const u32x4*)(base16 + ro + bj * 128); x0 = (f32x4){bflo(w.x), bfhi(w.x), bflo(w.y), bfhi(w.y)}; x1 = (f32x4){bflo(w.z), bfhi(w.z), bflo(w.w), bfhi(w.w)}; }
;                         const f32x4 v0 = x0 + g[bj][0] * acc[ai][bj][m][0], v1 = x1 + g[bj][1] * acc[ai][bj][m][1];
;                         acc[ai][bj][m][0] = v0; acc[ai][bj][m][1] = v1;
;                         u32x4 o; o.x = pk2(v0[0], v0[1]); o.y = pk2(v0[2], v0[3]); o.z = pk2(v1[0], v1[1]); o.w = pk2(v1[2], v1[3]);
;                         *(u32x4*)(X2 + ro + bj * 128) = o;
;                     }
.LBB0_1210:
	v_readlane_b32 s10, v250, 0
	v_readlane_b32 s11, v250, 1
	s_andn2_b64 vcc, exec, s[12:13]
	s_nop 0
	v_lshl_add_u64 v[202:203], v[204:205], 1, s[10:11]
	s_cbranch_vccnz .LBB0_1212
	global_load_dwordx4 v[154:157], v[202:203], off
	global_load_dwordx4 v[230:233], v[202:203], off offset:256
	s_waitcnt vmcnt(1)
	v_lshlrev_b32_e32 v158, 16, v154
	v_and_b32_e32 v159, 0xffff0000, v154
	v_lshlrev_b32_e32 v160, 16, v155
	v_and_b32_e32 v161, 0xffff0000, v155
	v_lshlrev_b32_e32 v154, 16, v156
	v_and_b32_e32 v155, 0xffff0000, v156
	v_lshlrev_b32_e32 v156, 16, v157
	v_and_b32_e32 v157, 0xffff0000, v157
.LBB0_1212:
	v_readlane_b32 s10, v249, 62
	v_readlane_b32 s11, v249, 63
	s_waitcnt vmcnt(2)
	v_pk_fma_f32 v[160:161], v[152:153], v[136:137], v[160:161]
	v_pk_fma_f32 v[158:159], v[150:151], v[134:135], v[158:159]
	v_pk_fma_f32 v[156:157], v[148:149], v[132:133], v[156:157]
	v_pk_fma_f32 v[154:155], v[146:147], v[130:131], v[154:155]
	v_lshl_add_u64 v[204:205], v[204:205], 1, s[10:11]
	s_and_b64 vcc, exec, s[34:35]
	v_cvt_pk_bf16_f32 v146, v158, v159
	v_cvt_pk_bf16_f32 v147, v160, v161
	v_cvt_pk_bf16_f32 v148, v154, v155
	v_cvt_pk_bf16_f32 v149, v156, v157
	global_store_dwordx4 v[204:205], v[146:149], off
	s_cbranch_vccnz .LBB0_1217
	s_nop 1
	s_waitcnt vmcnt(1)
	v_mov_b32_e32 v146, v230
	v_mov_b32_e32 v147, v231
	v_mov_b32_e32 v148, v232
	v_mov_b32_e32 v149, v233
	v_mov_b32_e32 v150, v234
	v_mov_b32_e32 v151, v235
	v_mov_b32_e32 v152, v236
	v_mov_b32_e32 v153, v237
	s_cbranch_execnz .LBB0_1215
.LBB0_1214:
	s_waitcnt vmcnt(1)
	v_lshlrev_b32_e32 v150, 16, v230
	v_and_b32_e32 v151, 0xffff0000, v230
	v_lshlrev_b32_e32 v152, 16, v231
	v_and_b32_e32 v153, 0xffff0000, v231
	v_lshlrev_b32_e32 v146, 16, v232
	v_and_b32_e32 v147, 0xffff0000, v232
	v_lshlrev_b32_e32 v148, 16, v233
	v_and_b32_e32 v149, 0xffff0000, v233
.LBB0_1215:
	s_waitcnt vmcnt(1)
	v_pk_fma_f32 v[150:151], v[142:143], v[98:99], v[150:151]
	v_pk_fma_f32 v[146:147], v[138:139], v[78:79], v[146:147]
	v_cvt_pk_bf16_f32 v138, v150, v151
	v_pk_fma_f32 v[152:153], v[144:145], v[100:101], v[152:153]
	v_pk_fma_f32 v[148:149], v[140:141], v[80:81], v[148:149]
	v_cvt_pk_bf16_f32 v139, v152, v153
	v_cvt_pk_bf16_f32 v140, v146, v147
	s_and_b64 vcc, exec, s[34:35]
	v_cvt_pk_bf16_f32 v141, v148, v149
	global_store_dwordx4 v[204:205], v[138:141], off offset:256
	s_nop 1
	v_or_b32_e32 v138, 48, v198
	v_ashrrev_i32_e32 v139, 31, v138
	v_lshlrev_b64 v[138:139], 11, v[138:139]
	v_lshl_add_u64 v[204:205], v[138:139], 0, v[196:197]
	v_lshl_add_u64 v[200:201], v[204:205], 2, s[40:41]
	s_cbranch_vccnz .LBB0_1218
	global_load_dwordx4 v[138:141], v[200:201], off offset:16
	global_load_dwordx4 v[142:145], v[200:201], off
	global_load_dwordx4 v[230:233], v[200:201], off offset:528
	global_load_dwordx4 v[234:237], v[200:201], off offset:512
	s_mov_b64 s[12:13], 0
	s_branch .LBB0_1219

; __device__ __forceinline__ unsigned pk2(float lo, float hi) { unsigned r; asm("v_cvt_pk_bf16_f32 %0, %1, %2" : "=v"(r) : "v"(lo), "v"(hi)); return r; }
; __device__ __forceinline__ float bflo(unsigned u) { return __uint_as_float(u << 16); }
; __device__ __forceinline__ float bfhi(unsigned u) { return __uint_as_float(u & 0xffff0000u); }
;     __device__ __forceinline__ void fused(AccT& acc, const GUnit& u, int wr, int wc, int fr, int fq, LAS unsigned char* lds, int wid, int lane) const {
;     ...
; #pragma unroll
;             for (int ai = 0; ai < 2; ++ai)
; #pragma unroll
;                 for (int m = 0; m < 4; ++m) {
;                     const size_t ro = (size_t)(u.pm * 256 + ai * 128 + wr * 64 + m * 16 + fr) * DM + col0;
; #pragma unroll
;                     for (int bj = 0; bj < 2; ++bj) {
;                         f32x4 x0, x1;
;                         if (base32) { x0 = *(const f32x4*)(base32 + ro + bj * 128); x1 = *(const f32x4*)(base32 + ro + bj * 128 + 4); }
;                         else { const u32x4 w = *(const u32x4*)(base16 + ro + bj * 128); x0 = (f32x4){bflo(w.x), bfhi(w.x), bflo(w.y), bfhi(w.y)}; x1 = (f32x4){bflo(w.z), bfhi(w.z), bflo(w.w), bfhi(w.w)}; }
;                         const f32x4 v0 = x0 + g[bj][0] * acc[ai][bj][m][0], v1 = x1 + g[bj][1] * acc[ai][bj][m][1];
;                         acc[ai][bj][m][0] = v0; acc[ai][bj][m][1] = v1;
;                         u32x4 o; o.x = pk2(v0[0], v0[1]); o.y = pk2(v0[2], v0[3]); o.z = pk2(v1[0], v1[1]); o.w = pk2(v1[2], v1[3]);
;                         *(u32x4*)(X2 + ro + bj * 128) = o;
;                     }
.LBB0_1219:
	v_readlane_b32 s10, v250, 0
	v_readlane_b32 s11, v250, 1
	s_andn2_b64 vcc, exec, s[12:13]
	s_nop 0
	v_lshl_add_u64 v[202:203], v[204:205], 1, s[10:11]
	s_cbranch_vccnz .LBB0_1221
	global_load_dwordx4 v[138:141], v[202:203], off
	global_load_dwordx4 v[230:233], v[202:203], off offset:256
	s_waitcnt vmcnt(1)
	v_lshlrev_b32_e32 v142, 16, v138
	v_and_b32_e32 v143, 0xffff0000, v138
	v_lshlrev_b32_e32 v144, 16, v139
	v_and_b32_e32 v145, 0xffff0000, v139
	v_lshlrev_b32_e32 v138, 16, v140
	v_and_b32_e32 v139, 0xffff0000, v140
	v_lshlrev_b32_e32 v140, 16, v141
	v_and_b32_e32 v141, 0xffff0000, v141
.LBB0_1221:
	v_readlane_b32 s10, v249, 62
	v_readlane_b32 s11, v249, 63
	s_waitcnt vmcnt(2)
	v_pk_fma_f32 v[144:145], v[128:129], v[136:137], v[144:145]
	v_pk_fma_f32 v[142:143], v[126:127], v[134:135], v[142:143]
	v_pk_fma_f32 v[140:141], v[124:125], v[132:133], v[140:141]
	v_pk_fma_f32 v[138:139], v[122:123], v[130:131], v[138:139]
	v_lshl_add_u64 v[204:205], v[204:205], 1, s[10:11]
	s_and_b64 vcc, exec, s[34:35]
	v_cvt_pk_bf16_f32 v122, v142, v143
	v_cvt_pk_bf16_f32 v123, v144, v145
	v_cvt_pk_bf16_f32 v124, v138, v139
	v_cvt_pk_bf16_f32 v125, v140, v141
	global_store_dwordx4 v[204:205], v[122:125], off
	s_cbranch_vccnz .LBB0_1226
	s_nop 1
	s_waitcnt vmcnt(1)
	v_mov_b32_e32 v122, v230
	v_mov_b32_e32 v123, v231
	v_mov_b32_e32 v124, v232
	v_mov_b32_e32 v125, v233
	v_mov_b32_e32 v126, v234
	v_mov_b32_e32 v127, v235
	v_mov_b32_e32 v128, v236
	v_mov_b32_e32 v129, v237
	s_cbranch_execnz .LBB0_1224
.LBB0_1223:
	s_waitcnt vmcnt(1)
	v_lshlrev_b32_e32 v126, 16, v230
	v_and_b32_e32 v127, 0xffff0000, v230
	v_lshlrev_b32_e32 v128, 16, v231
	v_and_b32_e32 v129, 0xffff0000, v231
	v_lshlrev_b32_e32 v122, 16, v232
	v_and_b32_e32 v123, 0xffff0000, v232
	v_lshlrev_b32_e32 v124, 16, v233
	v_and_b32_e32 v125, 0xffff0000, v233
.LBB0_1224:
	s_waitcnt vmcnt(1)
	v_pk_fma_f32 v[126:127], v[86:87], v[98:99], v[126:127]
	v_pk_fma_f32 v[122:123], v[74:75], v[78:79], v[122:123]
	v_cvt_pk_bf16_f32 v74, v126, v127
	v_pk_fma_f32 v[128:129], v[88:89], v[100:101], v[128:129]
	v_pk_fma_f32 v[124:125], v[76:77], v[80:81], v[124:125]
	v_cvt_pk_bf16_f32 v75, v128, v129
	v_cvt_pk_bf16_f32 v76, v122, v123
	s_and_b64 vcc, exec, s[34:35]
	v_cvt_pk_bf16_f32 v77, v124, v125
	global_store_dwordx4 v[204:205], v[74:77], off offset:256
	s_nop 1
	v_add_u32_e32 v74, 0x80, v198
	v_ashrrev_i32_e32 v75, 31, v74
	v_lshlrev_b64 v[74:75], 11, v[74:75]
	v_lshl_add_u64 v[204:205], v[74:75], 0, v[196:197]
	v_lshl_add_u64 v[200:201], v[204:205], 2, s[40:41]
	s_cbranch_vccnz .LBB0_1227
	global_load_dwordx4 v[74:77], v[200:201], off offset:16
	global_load_dwordx4 v[86:89], v[200:201], off
	global_load_dwordx4 v[230:233], v[200:201], off offset:528
	global_load_dwordx4 v[234:237], v[200:201], off offset:512
	s_mov_b64 s[12:13], 0
	s_branch .LBB0_1228

; __device__ __forceinline__ unsigned pk2(float lo, float hi) { unsigned r; asm("v_cvt_pk_bf16_f32 %0, %1, %2" : "=v"(r) : "v"(lo), "v"(hi)); return r; }
; __device__ __forceinline__ float bflo(unsigned u) { return __uint_as_float(u << 16); }
; __device__ __forceinline__ float bfhi(unsigned u) { return __uint_as_float(u & 0xffff0000u); }
;     __device__ __forceinline__ void fused(AccT& acc, const GUnit& u, int wr, int wc, int fr, int fq, LAS unsigned char* lds, int wid, int lane) const {
;     ...
; #pragma unroll
;             for (int ai = 0; ai < 2; ++ai)
; #pragma unroll
;                 for (int m = 0; m < 4; ++m) {
;                     const size_t ro = (size_t)(u.pm * 256 + ai * 128 + wr * 64 + m * 16 + fr) * DM + col0;
; #pragma unroll
;                     for (int bj = 0; bj < 2; ++bj) {
;                         f32x4 x0, x1;
;                         if (base32) { x0 = *(const f32x4*)(base32 + ro + bj * 128); x1 = *(const f32x4*)(base32 + ro + bj * 128 + 4); }
;                         else { const u32x4 w = *(const u32x4*)(base16 + ro + bj * 128); x0 = (f32x4){bflo(w.x), bfhi(w.x), bflo(w.y), bfhi(w.y)}; x1 = (f32x4){bflo(w.z), bfhi(w.z), bflo(w.w), bfhi(w.w)}; }
;                         const f32x4 v0 = x0 + g[bj][0] * acc[ai][bj][m][0], v1 = x1 + g[bj][1] * acc[ai][bj][m][1];
;                         acc[ai][bj][m][0] = v0; acc[ai][bj][m][1] = v1;
;                         u32x4 o; o.x = pk2(v0[0], v0[1]); o.y = pk2(v0[2], v0[3]); o.z = pk2(v1[0], v1[1]); o.w = pk2(v1[2], v1[3]);
;                         *(u32x4*)(X2 + ro + bj * 128) = o;
;                     }
.LBB0_1228:
	v_readlane_b32 s10, v250, 0
	v_readlane_b32 s11, v250, 1
	s_andn2_b64 vcc, exec, s[12:13]
	s_nop 0
	v_lshl_add_u64 v[202:203], v[204:205], 1, s[10:11]
	s_cbranch_vccnz .LBB0_1230
	global_load_dwordx4 v[74:77], v[202:203], off
	global_load_dwordx4 v[230:233], v[202:203], off offset:256
	s_waitcnt vmcnt(1)
	v_lshlrev_b32_e32 v86, 16, v74
	v_and_b32_e32 v87, 0xffff0000, v74
	v_lshlrev_b32_e32 v88, 16, v75
	v_and_b32_e32 v89, 0xffff0000, v75
	v_lshlrev_b32_e32 v74, 16, v76
	v_and_b32_e32 v75, 0xffff0000, v76
	v_lshlrev_b32_e32 v76, 16, v77
	v_and_b32_e32 v77, 0xffff0000, v77
.LBB0_1230:
	v_readlane_b32 s10, v249, 62
	v_readlane_b32 s11, v249, 63
	s_waitcnt vmcnt(2)
	v_pk_fma_f32 v[88:89], v[72:73], v[136:137], v[88:89]
	v_pk_fma_f32 v[86:87], v[70:71], v[134:135], v[86:87]
	v_pk_fma_f32 v[76:77], v[68:69], v[132:133], v[76:77]
	v_pk_fma_f32 v[74:75], v[66:67], v[130:131], v[74:75]
	v_lshl_add_u64 v[204:205], v[204:205], 1, s[10:11]
	s_and_b64 vcc, exec, s[34:35]
	v_cvt_pk_bf16_f32 v66, v86, v87
	v_cvt_pk_bf16_f32 v67, v88, v89
	v_cvt_pk_bf16_f32 v68, v74, v75
	v_cvt_pk_bf16_f32 v69, v76, v77
	global_store_dwordx4 v[204:205], v[66:69], off
	s_cbranch_vccnz .LBB0_1235
	s_nop 1
	s_waitcnt vmcnt(1)
	v_mov_b32_e32 v66, v230
	v_mov_b32_e32 v67, v231
	v_mov_b32_e32 v68, v232
	v_mov_b32_e32 v69, v233
	v_mov_b32_e32 v70, v234
	v_mov_b32_e32 v71, v235
	v_mov_b32_e32 v72, v236
	v_mov_b32_e32 v73, v237
	s_cbranch_execnz .LBB0_1233
.LBB0_1232:
	s_waitcnt vmcnt(1)
	v_lshlrev_b32_e32 v70, 16, v230
	v_and_b32_e32 v71, 0xffff0000, v230
	v_lshlrev_b32_e32 v72, 16, v231
	v_and_b32_e32 v73, 0xffff0000, v231
	v_lshlrev_b32_e32 v66, 16, v232
	v_and_b32_e32 v67, 0xffff0000, v232
	v_lshlrev_b32_e32 v68, 16, v233
	v_and_b32_e32 v69, 0xffff0000, v233
.LBB0_1233:
	s_waitcnt vmcnt(1)
	v_pk_fma_f32 v[70:71], v[62:63], v[98:99], v[70:71]
	v_pk_fma_f32 v[66:67], v[58:59], v[78:79], v[66:67]
	v_cvt_pk_bf16_f32 v58, v70, v71
	v_pk_fma_f32 v[72:73], v[64:65], v[100:101], v[72:73]
	v_pk_fma_f32 v[68:69], v[60:61], v[80:81], v[68:69]
	v_cvt_pk_bf16_f32 v59, v72, v73
	v_cvt_pk_bf16_f32 v60, v66, v67
	s_and_b64 vcc, exec, s[34:35]
	v_cvt_pk_bf16_f32 v61, v68, v69
	global_store_dwordx4 v[204:205], v[58:61], off offset:256
	s_nop 1
	v_add_u32_e32 v58, 0x90, v198
	v_ashrrev_i32_e32 v59, 31, v58
	v_lshlrev_b64 v[58:59], 11, v[58:59]
	v_lshl_add_u64 v[204:205], v[58:59], 0, v[196:197]
	v_lshl_add_u64 v[200:201], v[204:205], 2, s[40:41]
	s_cbranch_vccnz .LBB0_1236
	global_load_dwordx4 v[58:61], v[200:201], off offset:16
	global_load_dwordx4 v[62:65], v[200:201], off
	global_load_dwordx4 v[230:233], v[200:201], off offset:528
	global_load_dwordx4 v[234:237], v[200:201], off offset:512
	s_mov_b64 s[12:13], 0
	s_branch .LBB0_1237

; __device__ __forceinline__ unsigned pk2(float lo, float hi) { unsigned r; asm("v_cvt_pk_bf16_f32 %0, %1, %2" : "=v"(r) : "v"(lo), "v"(hi)); return r; }
; __device__ __forceinline__ float bflo(unsigned u) { return __uint_as_float(u << 16); }
; __device__ __forceinline__ float bfhi(unsigned u) { return __uint_as_float(u & 0xffff0000u); }
;     __device__ __forceinline__ void fused(AccT& acc, const GUnit& u, int wr, int wc, int fr, int fq, LAS unsigned char* lds, int wid, int lane) const {
;     ...
; #pragma unroll
;             for (int ai = 0; ai < 2; ++ai)
; #pragma unroll
;                 for (int m = 0; m < 4; ++m) {
;                     const size_t ro = (size_t)(u.pm * 256 + ai * 128 + wr * 64 + m * 16 + fr) * DM + col0;
; #pragma unroll
;                     for (int bj = 0; bj < 2; ++bj) {
;                         f32x4 x0, x1;
;                         if (base32) { x0 = *(const f32x4*)(base32 + ro + bj * 128); x1 = *(const f32x4*)(base32 + ro + bj * 128 + 4); }
;                         else { const u32x4 w = *(const u32x4*)(base16 + ro + bj * 128); x0 = (f32x4){bflo(w.x), bfhi(w.x), bflo(w.y), bfhi(w.y)}; x1 = (f32x4){bflo(w.z), bfhi(w.z), bflo(w.w), bfhi(w.w)}; }
;                         const f32x4 v0 = x0 + g[bj][0] * acc[ai][bj][m][0], v1 = x1 + g[bj][1] * acc[ai][bj][m][1];
;                         acc[ai][bj][m][0] = v0; acc[ai][bj][m][1] = v1;
;                         u32x4 o; o.x = pk2(v0[0], v0[1]); o.y = pk2(v0[2], v0[3]); o.z = pk2(v1[0], v1[1]); o.w = pk2(v1[2], v1[3]);
;                         *(u32x4*)(X2 + ro + bj * 128) = o;
;                     }
.LBB0_1237:
	v_readlane_b32 s10, v250, 0
	v_readlane_b32 s11, v250, 1
	s_andn2_b64 vcc, exec, s[12:13]
	s_nop 0
	v_lshl_add_u64 v[202:203], v[204:205], 1, s[10:11]
	s_cbranch_vccnz .LBB0_1239
	global_load_dwordx4 v[58:61], v[202:203], off
	global_load_dwordx4 v[230:233], v[202:203], off offset:256
	s_waitcnt vmcnt(1)
	v_lshlrev_b32_e32 v62, 16, v58
	v_and_b32_e32 v63, 0xffff0000, v58
	v_lshlrev_b32_e32 v64, 16, v59
	v_and_b32_e32 v65, 0xffff0000, v59
	v_lshlrev_b32_e32 v58, 16, v60
	v_and_b32_e32 v59, 0xffff0000, v60
	v_lshlrev_b32_e32 v60, 16, v61
	v_and_b32_e32 v61, 0xffff0000, v61
.LBB0_1239:
	v_readlane_b32 s10, v249, 62
	v_readlane_b32 s11, v249, 63
	s_waitcnt vmcnt(2)
	v_pk_fma_f32 v[64:65], v[56:57], v[136:137], v[64:65]
	v_pk_fma_f32 v[62:63], v[54:55], v[134:135], v[62:63]
	v_pk_fma_f32 v[60:61], v[48:49], v[132:133], v[60:61]
	v_pk_fma_f32 v[58:59], v[46:47], v[130:131], v[58:59]
	v_lshl_add_u64 v[204:205], v[204:205], 1, s[10:11]
	s_and_b64 vcc, exec, s[34:35]
	v_cvt_pk_bf16_f32 v46, v62, v63
	v_cvt_pk_bf16_f32 v47, v64, v65
	v_cvt_pk_bf16_f32 v48, v58, v59
	v_cvt_pk_bf16_f32 v49, v60, v61
	global_store_dwordx4 v[204:205], v[46:49], off
	s_cbranch_vccnz .LBB0_1244
	s_nop 1
	s_waitcnt vmcnt(1)
	v_mov_b32_e32 v46, v230
	v_mov_b32_e32 v47, v231
	v_mov_b32_e32 v48, v232
	v_mov_b32_e32 v49, v233
	v_mov_b32_e32 v54, v234
	v_mov_b32_e32 v55, v235
	v_mov_b32_e32 v56, v236
	v_mov_b32_e32 v57, v237
	s_cbranch_execnz .LBB0_1242
.LBB0_1241:
	s_waitcnt vmcnt(1)
	v_lshlrev_b32_e32 v54, 16, v230
	v_and_b32_e32 v55, 0xffff0000, v230
	v_lshlrev_b32_e32 v56, 16, v231
	v_and_b32_e32 v57, 0xffff0000, v231
	v_lshlrev_b32_e32 v46, 16, v232
	v_and_b32_e32 v47, 0xffff0000, v232
	v_lshlrev_b32_e32 v48, 16, v233
	v_and_b32_e32 v49, 0xffff0000, v233
.LBB0_1242:
	s_waitcnt vmcnt(1)
	v_pk_fma_f32 v[52:53], v[52:53], v[100:101], v[56:57]
	v_pk_fma_f32 v[50:51], v[50:51], v[98:99], v[54:55]
	v_pk_fma_f32 v[56:57], v[42:43], v[78:79], v[46:47]
	v_cvt_pk_bf16_f32 v42, v50, v51
	v_pk_fma_f32 v[54:55], v[44:45], v[80:81], v[48:49]
	v_cvt_pk_bf16_f32 v43, v52, v53
	v_cvt_pk_bf16_f32 v44, v56, v57
	s_and_b64 vcc, exec, s[34:35]
	v_cvt_pk_bf16_f32 v45, v54, v55
	global_store_dwordx4 v[204:205], v[42:45], off offset:256
	s_nop 1
	v_add_u32_e32 v42, 0xa0, v198
	v_ashrrev_i32_e32 v43, 31, v42
	v_lshlrev_b64 v[42:43], 11, v[42:43]
	v_lshl_add_u64 v[204:205], v[42:43], 0, v[196:197]
	v_lshl_add_u64 v[200:201], v[204:205], 2, s[40:41]
	s_cbranch_vccnz .LBB0_1245
	global_load_dwordx4 v[42:45], v[200:201], off offset:16
	global_load_dwordx4 v[46:49], v[200:201], off
	global_load_dwordx4 v[230:233], v[200:201], off offset:528
	global_load_dwordx4 v[234:237], v[200:201], off offset:512
	s_mov_b64 s[12:13], 0
	s_branch .LBB0_1246

; __device__ __forceinline__ unsigned pk2(float lo, float hi) { unsigned r; asm("v_cvt_pk_bf16_f32 %0, %1, %2" : "=v"(r) : "v"(lo), "v"(hi)); return r; }
; __device__ __forceinline__ float bflo(unsigned u) { return __uint_as_float(u << 16); }
; __device__ __forceinline__ float bfhi(unsigned u) { return __uint_as_float(u & 0xffff0000u); }
;     __device__ __forceinline__ void fused(AccT& acc, const GUnit& u, int wr, int wc, int fr, int fq, LAS unsigned char* lds, int wid, int lane) const {
;     ...
; #pragma unroll
;             for (int ai = 0; ai < 2; ++ai)
; #pragma unroll
;                 for (int m = 0; m < 4; ++m) {
;                     const size_t ro = (size_t)(u.pm * 256 + ai * 128 + wr * 64 + m * 16 + fr) * DM + col0;
; #pragma unroll
;                     for (int bj = 0; bj < 2; ++bj) {
;                         f32x4 x0, x1;
;                         if (base32) { x0 = *(const f32x4*)(base32 + ro + bj * 128); x1 = *(const f32x4*)(base32 + ro + bj * 128 + 4); }
;                         else { const u32x4 w = *(const u32x4*)(base16 + ro + bj * 128); x0 = (f32x4){bflo(w.x), bfhi(w.x), bflo(w.y), bfhi(w.y)}; x1 = (f32x4){bflo(w.z), bfhi(w.z), bflo(w.w), bfhi(w.w)}; }
;                         const f32x4 v0 = x0 + g[bj][0] * acc[ai][bj][m][0], v1 = x1 + g[bj][1] * acc[ai][bj][m][1];
;                         acc[ai][bj][m][0] = v0; acc[ai][bj][m][1] = v1;
;                         u32x4 o; o.x = pk2(v0[0], v0[1]); o.y = pk2(v0[2], v0[3]); o.z = pk2(v1[0], v1[1]); o.w = pk2(v1[2], v1[3]);
;                         *(u32x4*)(X2 + ro + bj * 128) = o;
;                     }
.LBB0_1246:
	v_readlane_b32 s10, v250, 0
	v_readlane_b32 s11, v250, 1
	s_andn2_b64 vcc, exec, s[12:13]
	s_nop 0
	v_lshl_add_u64 v[202:203], v[204:205], 1, s[10:11]
	s_cbranch_vccnz .LBB0_1248
	global_load_dwordx4 v[42:45], v[202:203], off
	global_load_dwordx4 v[230:233], v[202:203], off offset:256
	s_waitcnt vmcnt(1)
	v_lshlrev_b32_e32 v46, 16, v42
	v_and_b32_e32 v47, 0xffff0000, v42
	v_lshlrev_b32_e32 v48, 16, v43
	v_and_b32_e32 v49, 0xffff0000, v43
	v_lshlrev_b32_e32 v42, 16, v44
	v_and_b32_e32 v43, 0xffff0000, v44
	v_lshlrev_b32_e32 v44, 16, v45
	v_and_b32_e32 v45, 0xffff0000, v45
.LBB0_1248:
	v_readlane_b32 s10, v249, 62
	v_readlane_b32 s11, v249, 63
	s_waitcnt vmcnt(2)
	v_pk_fma_f32 v[48:49], v[36:37], v[136:137], v[48:49]
	v_pk_fma_f32 v[46:47], v[34:35], v[134:135], v[46:47]
	v_pk_fma_f32 v[44:45], v[28:29], v[132:133], v[44:45]
	v_pk_fma_f32 v[42:43], v[26:27], v[130:131], v[42:43]
	v_lshl_add_u64 v[204:205], v[204:205], 1, s[10:11]
	s_and_b64 vcc, exec, s[34:35]
	v_cvt_pk_bf16_f32 v26, v46, v47
	v_cvt_pk_bf16_f32 v27, v48, v49
	v_cvt_pk_bf16_f32 v28, v42, v43
	v_cvt_pk_bf16_f32 v29, v44, v45
	global_store_dwordx4 v[204:205], v[26:29], off
	s_cbranch_vccnz .LBB0_1253
	s_nop 1
	s_waitcnt vmcnt(1)
	v_mov_b32_e32 v26, v230
	v_mov_b32_e32 v27, v231
	v_mov_b32_e32 v28, v232
	v_mov_b32_e32 v29, v233
	v_mov_b32_e32 v34, v234
	v_mov_b32_e32 v35, v235
	v_mov_b32_e32 v36, v236
	v_mov_b32_e32 v37, v237
	s_cbranch_execnz .LBB0_1251
.LBB0_1250:
	s_waitcnt vmcnt(1)
	v_lshlrev_b32_e32 v34, 16, v230
	v_and_b32_e32 v35, 0xffff0000, v230
	v_lshlrev_b32_e32 v36, 16, v231
	v_and_b32_e32 v37, 0xffff0000, v231
	v_lshlrev_b32_e32 v26, 16, v232
	v_and_b32_e32 v27, 0xffff0000, v232
	v_lshlrev_b32_e32 v28, 16, v233
	v_and_b32_e32 v29, 0xffff0000, v233
.LBB0_1251:
	s_waitcnt vmcnt(1)
	v_pk_fma_f32 v[36:37], v[40:41], v[100:101], v[36:37]
	v_pk_fma_f32 v[34:35], v[38:39], v[98:99], v[34:35]
	v_pk_fma_f32 v[40:41], v[30:31], v[78:79], v[26:27]
	v_cvt_pk_bf16_f32 v26, v34, v35
	v_pk_fma_f32 v[38:39], v[32:33], v[80:81], v[28:29]
	v_cvt_pk_bf16_f32 v27, v36, v37
	v_cvt_pk_bf16_f32 v28, v40, v41
	s_and_b64 vcc, exec, s[34:35]
	v_cvt_pk_bf16_f32 v29, v38, v39
	global_store_dwordx4 v[204:205], v[26:29], off offset:256
	s_nop 1
	v_add_u32_e32 v26, 0xb0, v198
	v_ashrrev_i32_e32 v27, 31, v26
	v_lshlrev_b64 v[26:27], 11, v[26:27]
	v_lshl_add_u64 v[202:203], v[26:27], 0, v[196:197]
	v_lshl_add_u64 v[198:199], v[202:203], 2, s[40:41]
	s_cbranch_vccnz .LBB0_1254
	global_load_dwordx4 v[26:29], v[198:199], off offset:16
	global_load_dwordx4 v[30:33], v[198:199], off
	global_load_dwordx4 v[230:233], v[198:199], off offset:528
	global_load_dwordx4 v[234:237], v[198:199], off offset:512
	s_mov_b64 s[12:13], 0
	s_branch .LBB0_1255

; __device__ __forceinline__ unsigned pk2(float lo, float hi) { unsigned r; asm("v_cvt_pk_bf16_f32 %0, %1, %2" : "=v"(r) : "v"(lo), "v"(hi)); return r; }
; __device__ __forceinline__ float bflo(unsigned u) { return __uint_as_float(u << 16); }
;     __device__ __forceinline__ void fused(AccT& acc, const GUnit& u, int wr, int wc, int fr, int fq, LAS unsigned char* lds, int wid, int lane) const {
;     ...
;                     for (int bj = 0; bj < 2; ++bj) {
;                         f32x4 x0, x1;
;                         if (base32) { x0 = *(const f32x4*)(base32 + ro + bj * 128); x1 = *(const f32x4*)(base32 + ro + bj * 128 + 4); }
;                         else { const u32x4 w = *(const u32x4*)(base16 + ro + bj * 128); x0 = (f32x4){bflo(w.x), bfhi(w.x), bflo(w.y), bfhi(w.y)}; x1 = (f32x4){bflo(w.z), bfhi(w.z), bflo(w.w), bfhi(w.w)}; }
;                         const f32x4 v0 = x0 + g[bj][0] * acc[ai][bj][m][0], v1 = x1 + g[bj][1] * acc[ai][bj][m][1];
;                         acc[ai][bj][m][0] = v0; acc[ai][bj][m][1] = v1;
;                         u32x4 o; o.x = pk2(v0[0], v0[1]); o.y = pk2(v0[2], v0[3]); o.z = pk2(v1[0], v1[1]); o.w = pk2(v1[2], v1[3]);
;                         *(u32x4*)(X2 + ro + bj * 128) = o;
;                     }
;     ...
;             for (int ai = 0; ai < 2; ++ai)
; #pragma unroll
;                 for (int m = 0; m < 4; ++m) {
;                     const int rowl = ai * 128 + wr * 64 + m * 16;
;                     float sq = 0.f; f32x4 lg = (f32x4){0.f, 0.f, 0.f, 0.f};
; #pragma unroll
;                     for (int bj = 0; bj < 2; ++bj) {
;                         const f32x4 x0 = acc[ai][bj][m][0], x1 = acc[ai][bj][m][1];
;                         sq += (x0[0] * x0[0] + x0[1] * x0[1]) + (x0[2] * x0[2] + x0[3] * x0[3]) + (x1[0] * x1[0] + x1[1] * x1[1]) + (x1[2] * x1[2] + x1[3] * x1[3]);
;                         const f32x4 h0 = x0 * G[bj][0], h1 = x1 * G[bj][1];
;                         lg = __builtin_amdgcn_mfma_f32_16x16x32_bf16(pack8(h0[0], h0[1], h0[2], h0[3], h1[0], h1[1], h1[2], h1[3]), wf[bj], lg, 0, 0, 0);
;                     }
;                     sq += __shfl_xor(sq, 16); sq += __shfl_xor(sq, 32);
;                     if (fq == 0) P[(rowl + fr) * 4 + wc] = sq;
; #pragma unroll
;                     for (int i = 0; i < 4; ++i) LP[((size_t)wc * 256 + rowl + 4 * fq + i) * 16 + fr] = lg[i];
.LBB0_1255:
	v_readlane_b32 s10, v250, 0
	v_readlane_b32 s11, v250, 1
	s_andn2_b64 vcc, exec, s[12:13]
	s_nop 0
	v_lshl_add_u64 v[200:201], v[202:203], 1, s[10:11]
	s_cbranch_vccnz .LBB0_1257
	global_load_dwordx4 v[26:29], v[200:201], off
	global_load_dwordx4 v[230:233], v[200:201], off offset:256
	s_waitcnt vmcnt(1)
	v_lshlrev_b32_e32 v30, 16, v26
	v_and_b32_e32 v31, 0xffff0000, v26
	v_lshlrev_b32_e32 v32, 16, v27
	v_and_b32_e32 v33, 0xffff0000, v27
	v_lshlrev_b32_e32 v26, 16, v28
	v_and_b32_e32 v27, 0xffff0000, v28
	v_lshlrev_b32_e32 v28, 16, v29
	v_and_b32_e32 v29, 0xffff0000, v29
.LBB0_1257:
	v_readlane_b32 s10, v249, 62
	v_readlane_b32 s11, v249, 63
	s_waitcnt vmcnt(2)
	v_pk_fma_f32 v[32:33], v[24:25], v[136:137], v[32:33]
	v_pk_fma_f32 v[30:31], v[22:23], v[134:135], v[30:31]
	v_pk_fma_f32 v[28:29], v[20:21], v[132:133], v[28:29]
	v_pk_fma_f32 v[26:27], v[18:19], v[130:131], v[26:27]
	v_lshl_add_u64 v[130:131], v[202:203], 1, s[10:11]
	s_and_b64 vcc, exec, s[34:35]
	v_cvt_pk_bf16_f32 v18, v30, v31
	v_cvt_pk_bf16_f32 v19, v32, v33
	v_cvt_pk_bf16_f32 v20, v26, v27
	v_cvt_pk_bf16_f32 v21, v28, v29
	global_store_dwordx4 v[130:131], v[18:21], off
	s_cbranch_vccnz .LBB0_1315
	s_nop 1
	s_waitcnt vmcnt(1)
	v_mov_b32_e32 v18, v230
	v_mov_b32_e32 v19, v231
	v_mov_b32_e32 v20, v232
	v_mov_b32_e32 v21, v233
	v_mov_b32_e32 v22, v234
	v_mov_b32_e32 v23, v235
	v_mov_b32_e32 v24, v236
	v_mov_b32_e32 v25, v237
	s_cbranch_execnz .LBB0_1260
.LBB0_1259:
	s_waitcnt vmcnt(1)
	v_lshlrev_b32_e32 v22, 16, v230
	v_and_b32_e32 v23, 0xffff0000, v230
	v_lshlrev_b32_e32 v24, 16, v231
	v_and_b32_e32 v25, 0xffff0000, v231
	v_lshlrev_b32_e32 v18, 16, v232
	v_and_b32_e32 v19, 0xffff0000, v232
	v_lshlrev_b32_e32 v20, 16, v233
	v_and_b32_e32 v21, 0xffff0000, v233
.LBB0_1260:
	s_waitcnt vmcnt(1)
	v_pk_fma_f32 v[24:25], v[16:17], v[100:101], v[24:25]
	v_pk_fma_f32 v[22:23], v[14:15], v[98:99], v[22:23]
	v_pk_fma_f32 v[18:19], v[10:11], v[78:79], v[18:19]
	v_cvt_pk_bf16_f32 v10, v22, v23
	v_cvt_pk_bf16_f32 v11, v24, v25
	v_pk_fma_f32 v[20:21], v[12:13], v[80:81], v[20:21]
	v_cvt_pk_bf16_f32 v12, v18, v19
	v_pk_add_f32 v[120:121], v[120:121], 1.0 op_sel_hi:[1,0]
	v_cvt_pk_bf16_f32 v13, v20, v21
	global_store_dwordx4 v[130:131], v[10:13], off offset:256
	v_pk_add_f32 v[118:119], v[118:119], 1.0 op_sel_hi:[1,0]
	v_pk_mul_f32 v[116:117], v[116:117], v[120:121]
	v_mul_f32_e32 v10, v191, v191
	v_mul_f32_e32 v11, v193, v193
	v_fmac_f32_e32 v10, v190, v190
	v_fmac_f32_e32 v11, v192, v192
	v_add_f32_e32 v10, v10, v11
	v_mul_f32_e32 v11, v187, v187
	v_fmac_f32_e32 v11, v186, v186
	v_pk_mul_f32 v[114:115], v[114:115], v[118:119]
	v_pk_add_f32 v[118:119], v[106:107], 1.0 op_sel_hi:[1,0]
	v_pk_add_f32 v[106:107], v[108:109], 1.0 op_sel_hi:[1,0]
	v_add_f32_e32 v10, v11, v10
	v_mul_f32_e32 v11, v189, v189
	v_pk_mul_f32 v[106:107], v[96:97], v[106:107]
	v_pk_mul_f32 v[108:109], v[94:95], v[118:119]
	v_pk_add_f32 v[90:91], v[90:91], 1.0 op_sel_hi:[1,0]
	v_fmac_f32_e32 v11, v188, v188
	v_pk_mul_f32 v[14:15], v[116:117], v[192:193]
	v_pk_mul_f32 v[82:83], v[82:83], v[90:91]
	v_add_f32_e32 v90, v11, v10
	v_pk_mul_f32 v[16:17], v[114:115], v[190:191]
	v_pk_mul_f32 v[78:79], v[106:107], v[188:189]
	v_pk_mul_f32 v[80:81], v[108:109], v[186:187]
	v_cmp_lt_i32_e64 s[34:35], v216, v213
	v_cvt_pk_bf16_f32 v10, v16, v17
	v_cvt_pk_bf16_f32 v11, v14, v15
	v_cvt_pk_bf16_f32 v12, v80, v81
	v_cvt_pk_bf16_f32 v13, v78, v79
	s_nop 1
	v_mul_f32_e32 v14, v183, v183
	v_mul_f32_e32 v15, v185, v185
	v_fmac_f32_e32 v14, v182, v182
	v_fmac_f32_e32 v15, v184, v184
	v_add_f32_e32 v14, v14, v15
	v_mul_f32_e32 v15, v179, v179
	v_fmac_f32_e32 v15, v178, v178
	v_add_f32_e32 v14, v15, v14
	v_mul_f32_e32 v15, v181, v181
	v_fmac_f32_e32 v15, v180, v180
	v_add_f32_e32 v14, v15, v14
	v_add_f32_e32 v15, v90, v14
	v_cndmask_b32_e64 v14, v212, v216, s[34:35]
	v_pk_add_f32 v[94:95], v[112:113], 1.0 op_sel_hi:[1,0]
	v_lshlrev_b32_e32 v14, 2, v14
	v_pk_add_f32 v[96:97], v[110:111], 1.0 op_sel_hi:[1,0]
	v_pk_mul_f32 v[94:95], v[104:105], v[94:95]
	v_pk_add_f32 v[92:93], v[92:93], 1.0 op_sel_hi:[1,0]
	v_mov_b32_e32 v100, v15
	s_nop 1
	v_permlane16_swap_b32_e32 v15, v100
	v_pk_mul_f32 v[96:97], v[102:103], v[96:97]
	v_pk_mul_f32 v[84:85], v[84:85], v[92:93]
	v_pk_mul_f32 v[16:17], v[94:95], v[184:185]
	v_pk_mul_f32 v[90:91], v[96:97], v[182:183]
	v_pk_mul_f32 v[92:93], v[84:85], v[180:181]
	v_pk_mul_f32 v[98:99], v[82:83], v[178:179]
	v_mfma_f32_16x16x32_bf16 v[10:13], v[10:13], v[6:9], 0
	v_cvt_pk_bf16_f32 v78, v90, v91
	v_cvt_pk_bf16_f32 v79, v16, v17
	v_cvt_pk_bf16_f32 v80, v98, v99
	v_cvt_pk_bf16_f32 v81, v92, v93
	s_nop 1
	v_xor_b32_e32 v16, 32, v212
	v_cmp_lt_i32_e64 s[34:35], v16, v213
	s_waitcnt lgkmcnt(0)
	v_add_f32_e32 v15, v15, v100
	v_mfma_f32_16x16x32_bf16 v[10:13], v[78:81], v[2:5], v[10:13]
	v_cndmask_b32_e64 v16, v212, v16, s[34:35]
	v_lshlrev_b32_e32 v17, 2, v16
	ds_bpermute_b32 v16, v17, v15
	v_and_b32_e32 v132, 63, v207
	s_lshl_b32 s10, s59, 2
	s_add_i32 s10, s10, 0
	v_cmp_gt_u32_e32 vcc, 16, v132
	s_and_saveexec_b64 s[12:13], vcc
	s_cbranch_execz .LBB0_1262
	v_lshl_add_u32 v78, v1, 4, s10
	s_waitcnt lgkmcnt(0)
	v_add_f32_e32 v15, v15, v16
	ds_write_b32 v78, v15
